# baseline (speedup 1.0000x reference)
.Lstag_loop_p1:
	s_sleep 8
	s_add_i32 s20, s20, -1
	s_cmp_lg_u32 s20, 0
	s_cbranch_scc1 .Lstag_loop_p1
